# speedup vs baseline: 1.0032x; 1.0032x over previous
_Z11attn_kernelPKDF16_S0_S0_PfPDF16_S1_:
	v_and_b32_e32 v65, 63, v0
	s_lshl_b32 s3, s2, 7
	s_lshr_b32 s4, s2, 2
	s_and_b32 s3, s3, 0x180
	s_and_b32 s4, s4, 0x3ffffffe
	s_add_i32 s3, s3, s4
	s_bfe_u32 s2, s2, 0x10002
	s_or_b32 s40, s3, s2
	s_mov_b32 s41, 0
	s_lshl_b64 s[2:3], s[40:41], 2
	s_getpc_b64 s[4:5]
	s_add_u32 s4, s4, g_tab@rel32@lo+4
	s_addc_u32 s5, s5, g_tab@rel32@hi+12
	s_add_u32 s42, s4, s2
	s_addc_u32 s43, s5, s3
	s_load_dword s12, s[42:43], 0x0
	s_load_dwordx4 s[4:7], s[0:1], 0x8
	s_load_dword s76, s[42:43], 0x1000
	s_load_dwordx2 s[80:81], s[0:1], 0x0
	s_load_dwordx4 s[84:87], s[0:1], 0x18
	s_load_dwordx2 s[88:89], s[0:1], 0x28
	v_lshlrev_b32_e32 v2, 4, v0
	s_movk_i32 s8, 0x70
	v_readfirstlane_b32 s3, v0
	s_waitcnt lgkmcnt(0)
	s_add_u32 s70, s4, 0x2000
	s_addc_u32 s71, s5, 0
	s_add_u32 s72, s6, 0x2000
	s_addc_u32 s73, s7, 0
	s_and_b32 s2, s12, 3
	s_lshl_b32 s10, s2, 19
	v_bitop3_b32 v10, v2, s8, v0 bitop3:0x48
	s_add_u32 s8, s6, s10
	s_addc_u32 s9, s7, 0
	s_lshr_b32 s13, s3, 6
	s_bfe_u32 s40, s12, 0x70007
	s_bfe_u32 s33, s12, 0x6000e
	v_and_b32_e32 v1, 0x1f80, v2
	s_add_u32 s10, s4, s10
	v_or_b32_e32 v50, v10, v1
	v_mov_b32_e32 v51, 0
	s_addc_u32 s11, s5, 0
	v_lshl_add_u64 v[52:53], s[10:11], 0, v[50:51]
	v_lshl_add_u64 v[54:55], s[8:9], 0, v[50:51]
	s_lshl_b32 s8, s40, 13
	s_mov_b32 s9, s41
	s_lshl_b32 s50, s13, 10
	v_lshl_add_u64 v[2:3], v[52:53], 0, s[8:9]
	s_mov_b32 m0, s50
	s_add_i32 s51, s50, 0x2000
	global_load_lds_dwordx4 v[2:3], off
	v_lshl_add_u64 v[2:3], v[54:55], 0, s[8:9]
	s_mov_b32 m0, s51
	s_cmp_eq_u32 s33, 0
	global_load_lds_dwordx4 v[2:3], off
	s_cbranch_scc1 .LBB2_30
	s_mov_b64 s[14:15], s[80:81]
	s_mov_b64 s[8:9], s[84:85]
	s_mov_b64 s[10:11], s[86:87]
	s_mov_b64 s[44:45], s[88:89]
	s_cmp_ge_u32 s13, 4
	s_cbranch_scc1 .Lattn_prio_done
	s_setprio 1
